# peel+trim + attention running max as two v_max3 chains (16 instead of 53 VALU per tile)
# speedup vs baseline: 1.0029x; 1.0029x over previous
.LBB0_827:
	s_nop 10
	v_max3_f32 v2, v36, v37, v38
	v_max3_f32 v152, v52, v53, v54
	v_max3_f32 v2, v2, v39, v40
	v_max3_f32 v152, v152, v55, v56
	v_max3_f32 v2, v2, v41, v42
	v_max3_f32 v152, v152, v57, v58
	v_max3_f32 v2, v2, v43, v44
	v_max3_f32 v152, v152, v59, v60
	v_max3_f32 v2, v2, v45, v46
	v_max3_f32 v152, v152, v61, v62
	v_max3_f32 v2, v2, v47, v48
	v_max3_f32 v152, v152, v63, v64
	v_max3_f32 v2, v2, v49, v50
	v_max3_f32 v152, v152, v65, v66
	v_max3_f32 v2, v2, v51, v67
	v_max_f32_e32 v2, v2, v152
	v_and_b32_e32 v153, 64, v250
	v_xor_b32_e32 v152, 32, v250
	v_add_u32_e32 v153, 64, v153
	v_cmp_lt_i32_e32 vcc, v152, v153
	s_nop 1
	v_cndmask_b32_e32 v152, v250, v152, vcc
	v_lshlrev_b32_e32 v152, 2, v152
	ds_bpermute_b32 v153, v152, v2
	s_waitcnt lgkmcnt(0)
	v_max3_f32 v2, v151, v2, v153
	v_cmp_gt_f32_e32 vcc, v2, v151
	s_cbranch_vccz .LBB0_829
	v_sub_f32_e32 v151, v151, v2
	v_mul_f32_e32 v151, 0x3e16c740, v151
	v_exp_f32_e32 v154, v151
	s_nop 0
	v_mul_f32_e32 v135, v135, v154
	v_pk_mul_f32 v[34:35], v[34:35], v[154:155] op_sel_hi:[1,0]
	v_pk_mul_f32 v[32:33], v[32:33], v[154:155] op_sel_hi:[1,0]
	v_pk_mul_f32 v[30:31], v[30:31], v[154:155] op_sel_hi:[1,0]
	v_pk_mul_f32 v[28:29], v[28:29], v[154:155] op_sel_hi:[1,0]
	v_pk_mul_f32 v[26:27], v[26:27], v[154:155] op_sel_hi:[1,0]
	v_pk_mul_f32 v[24:25], v[24:25], v[154:155] op_sel_hi:[1,0]
	v_pk_mul_f32 v[22:23], v[22:23], v[154:155] op_sel_hi:[1,0]
	v_pk_mul_f32 v[20:21], v[20:21], v[154:155] op_sel_hi:[1,0]
	v_pk_mul_f32 v[18:19], v[18:19], v[154:155] op_sel_hi:[1,0]
	v_pk_mul_f32 v[16:17], v[16:17], v[154:155] op_sel_hi:[1,0]
	v_pk_mul_f32 v[14:15], v[14:15], v[154:155] op_sel_hi:[1,0]
	v_pk_mul_f32 v[12:13], v[12:13], v[154:155] op_sel_hi:[1,0]
	v_pk_mul_f32 v[10:11], v[10:11], v[154:155] op_sel_hi:[1,0]
	v_pk_mul_f32 v[8:9], v[8:9], v[154:155] op_sel_hi:[1,0]
	v_pk_mul_f32 v[6:7], v[6:7], v[154:155] op_sel_hi:[1,0]
	v_pk_mul_f32 v[4:5], v[4:5], v[154:155] op_sel_hi:[1,0]

.LBB0_843:
	s_nop 10
	v_max3_f32 v69, v36, v37, v38
	v_max3_f32 v68, v52, v53, v54
	v_max3_f32 v69, v69, v39, v40
	v_max3_f32 v68, v68, v55, v56
	v_max3_f32 v69, v69, v41, v42
	v_max3_f32 v68, v68, v57, v58
	v_max3_f32 v69, v69, v43, v44
	v_max3_f32 v68, v68, v59, v60
	v_max3_f32 v69, v69, v45, v46
	v_max3_f32 v68, v68, v61, v62
	v_max3_f32 v69, v69, v47, v48
	v_max3_f32 v68, v68, v63, v64
	v_max3_f32 v69, v69, v49, v50
	v_max3_f32 v68, v68, v65, v66
	v_max3_f32 v69, v69, v51, v67
	v_max_f32_e32 v69, v69, v68
	v_and_b32_e32 v70, 64, v250
	v_xor_b32_e32 v68, 32, v250
	v_add_u32_e32 v70, 64, v70
	v_cmp_lt_i32_e32 vcc, v68, v70
	s_nop 1
	v_cndmask_b32_e32 v68, v250, v68, vcc
	v_lshlrev_b32_e32 v68, 2, v68
	ds_bpermute_b32 v70, v68, v69
	s_waitcnt lgkmcnt(0)
	v_max3_f32 v69, v2, v69, v70
	v_cmp_gt_f32_e32 vcc, v69, v2
	s_cbranch_vccz .LBB0_845
	v_sub_f32_e32 v2, v2, v69
	v_mul_f32_e32 v2, 0x3e16c740, v2
	v_exp_f32_e32 v2, v2
	s_nop 0
	v_mul_f32_e32 v135, v135, v2
	v_pk_mul_f32 v[34:35], v[34:35], v[2:3] op_sel_hi:[1,0]
	v_pk_mul_f32 v[32:33], v[32:33], v[2:3] op_sel_hi:[1,0]
	v_pk_mul_f32 v[30:31], v[30:31], v[2:3] op_sel_hi:[1,0]
	v_pk_mul_f32 v[28:29], v[28:29], v[2:3] op_sel_hi:[1,0]
	v_pk_mul_f32 v[26:27], v[26:27], v[2:3] op_sel_hi:[1,0]
	v_pk_mul_f32 v[24:25], v[24:25], v[2:3] op_sel_hi:[1,0]
	v_pk_mul_f32 v[22:23], v[22:23], v[2:3] op_sel_hi:[1,0]
	v_pk_mul_f32 v[20:21], v[20:21], v[2:3] op_sel_hi:[1,0]
	v_pk_mul_f32 v[18:19], v[18:19], v[2:3] op_sel_hi:[1,0]
	v_pk_mul_f32 v[16:17], v[16:17], v[2:3] op_sel_hi:[1,0]
	v_pk_mul_f32 v[14:15], v[14:15], v[2:3] op_sel_hi:[1,0]
	v_pk_mul_f32 v[12:13], v[12:13], v[2:3] op_sel_hi:[1,0]
	v_pk_mul_f32 v[10:11], v[10:11], v[2:3] op_sel_hi:[1,0]
	v_pk_mul_f32 v[8:9], v[8:9], v[2:3] op_sel_hi:[1,0]
	v_pk_mul_f32 v[6:7], v[6:7], v[2:3] op_sel_hi:[1,0]
	v_pk_mul_f32 v[4:5], v[4:5], v[2:3] op_sel_hi:[1,0]
